# RWKV CUs: prep wave 4 (the scan wave's SIMD partner) idles, six prep waves deal all blocks; poll hoist, prep-wait removal, GEMM peel kept
# speedup vs baseline: 1.0120x; 1.0053x over previous
.LBB0_957:
	s_andn2_b64 vcc, exec, s[20:21]
	s_cbranch_vccnz .LBB0_879
	v_readlane_b32 s8, v253, 1
	v_readlane_b32 s9, v253, 2
	s_mov_b64 s[20:21], -1
	s_and_b64 vcc, exec, s[8:9]
	s_cbranch_vccz .LBB0_1002
	v_readlane_b32 s8, v255, 8
	s_nop 3
	s_cmp_eq_u32 s8, 4
	s_cbranch_scc1 .LBB0_879
	v_mov_b32_e32 v0, 0
	s_and_saveexec_b64 s[20:21], s[36:37]
	s_cbranch_execz .LBB0_963
	s_mov_b64 s[30:31], exec
	v_mbcnt_lo_u32_b32 v0, s30, 0
	v_mbcnt_hi_u32_b32 v0, s31, v0
	v_cmp_eq_u32_e32 vcc, 0, v0
	s_and_saveexec_b64 s[26:27], vcc
	s_cbranch_execz .LBB0_962
	s_bcnt1_i32_b64 s8, s[30:31]
	v_readlane_b32 s9, v255, 15
	v_mov_b32_e32 v2, s8
	s_nop 0
	v_mov_b32_e32 v1, s9
	ds_add_rtn_u32 v1, v1, v2
